# GQA post-loop P*V sections: counted waits per MFMA instead of lgkmcnt(0) per group, on top of v75
# baseline (speedup 1.0000x reference)
.LBB0_856:
	ds_read_b128 v[64:67], v177 offset:49152
	ds_read_b128 v[68:71], v177 offset:57344
	s_waitcnt lgkmcnt(1)
	v_mfma_f32_32x32x16_bf16 v[80:95], v[64:67], v[126:129], 0
	s_waitcnt lgkmcnt(0)
	v_mfma_f32_32x32x16_bf16 v[64:79], v[68:71], v[126:129], 0
	ds_read_b128 v[126:129], v178 offset:49152
	ds_read_b128 v[204:207], v178 offset:57344
	s_waitcnt lgkmcnt(1)
	v_mfma_f32_32x32x16_bf16 v[80:95], v[126:129], v[122:125], v[80:95]
	s_waitcnt lgkmcnt(0)
	v_mfma_f32_32x32x16_bf16 v[64:79], v[204:207], v[122:125], v[64:79]
	ds_read_b128 v[122:125], v179 offset:49152
	ds_read_b128 v[126:129], v179 offset:57344
	s_waitcnt lgkmcnt(1)
	v_mfma_f32_32x32x16_bf16 v[80:95], v[122:125], v[118:121], v[80:95]
	s_waitcnt lgkmcnt(0)
	v_mfma_f32_32x32x16_bf16 v[64:79], v[126:129], v[118:121], v[64:79]
	ds_read_b128 v[118:121], v180 offset:49152
	ds_read_b128 v[122:125], v180 offset:57344
	s_waitcnt lgkmcnt(1)
	v_mfma_f32_32x32x16_bf16 v[80:95], v[118:121], v[114:117], v[80:95]
	s_waitcnt lgkmcnt(0)
	v_mfma_f32_32x32x16_bf16 v[64:79], v[122:125], v[114:117], v[64:79]
	ds_read_b128 v[114:117], v181 offset:49152
	ds_read_b128 v[118:121], v181 offset:57344
	v_exp_f32_e32 v122, v136
	v_exp_f32_e32 v123, v137
	s_waitcnt lgkmcnt(1)
	v_mfma_f32_32x32x16_bf16 v[80:95], v[114:117], v[110:113], v[80:95]
	s_waitcnt lgkmcnt(0)
	v_mfma_f32_32x32x16_bf16 v[64:79], v[118:121], v[110:113], v[64:79]
	ds_read_b128 v[110:113], v182 offset:49152
	ds_read_b128 v[114:117], v182 offset:57344
	v_exp_f32_e32 v118, v144
	v_exp_f32_e32 v119, v145
	v_exp_f32_e32 v120, v138
	v_exp_f32_e32 v121, v139
	s_waitcnt lgkmcnt(1)
	v_mfma_f32_32x32x16_bf16 v[80:95], v[110:113], v[106:109], v[80:95]
	s_waitcnt lgkmcnt(0)
	v_mfma_f32_32x32x16_bf16 v[64:79], v[114:117], v[106:109], v[64:79]
	ds_read_b128 v[106:109], v183 offset:49152
	ds_read_b128 v[110:113], v183 offset:57344
	v_exp_f32_e32 v114, v132
	v_exp_f32_e32 v115, v133
	v_exp_f32_e32 v116, v130
	v_exp_f32_e32 v117, v131
	s_waitcnt lgkmcnt(1)
	v_mfma_f32_32x32x16_bf16 v[80:95], v[106:109], v[102:105], v[80:95]
	s_waitcnt lgkmcnt(0)
	v_mfma_f32_32x32x16_bf16 v[64:79], v[110:113], v[102:105], v[64:79]
	ds_read_b128 v[102:105], v184 offset:49152
	ds_read_b128 v[106:109], v184 offset:57344
	v_exp_f32_e32 v110, v140
	v_exp_f32_e32 v111, v141
	v_exp_f32_e32 v112, v134
	v_exp_f32_e32 v113, v135
	s_waitcnt lgkmcnt(1)
	v_mfma_f32_32x32x16_bf16 v[80:95], v[102:105], v[98:101], v[80:95]
	v_cvt_pk_bf16_f32 v102, v224, v225
	v_cvt_pk_bf16_f32 v103, v201, v203
	v_cvt_pk_bf16_f32 v104, v196, v198
	v_cvt_pk_bf16_f32 v105, v199, v200
	s_waitcnt lgkmcnt(0)
	v_mfma_f32_32x32x16_bf16 v[64:79], v[106:109], v[98:101], v[64:79]
	v_add_f32_e32 v98, 0, v202
	v_add_f32_e32 v98, v221, v98
	v_add_f32_e32 v98, v222, v98
	v_add_f32_e32 v98, v223, v98
	v_add_f32_e32 v98, v224, v98
	v_add_f32_e32 v98, v225, v98
	v_add_f32_e32 v98, v201, v98
	v_add_f32_e32 v98, v203, v98
	v_add_f32_e32 v98, v196, v98
	v_add_f32_e32 v98, v198, v98
	v_add_f32_e32 v98, v199, v98
	v_add_f32_e32 v98, v200, v98
	v_exp_f32_e32 v108, v142
	v_add_f32_e32 v98, v193, v98
	v_exp_f32_e32 v109, v143
	v_add_f32_e32 v98, v194, v98
	v_add_f32_e32 v98, v195, v98
	v_add_f32_e32 v98, v197, v98
	v_add_f32_e32 v98, v108, v98
	v_add_f32_e32 v98, v109, v98
	v_add_f32_e32 v98, v110, v98
	v_add_f32_e32 v98, v111, v98
	v_add_f32_e32 v98, v112, v98
	v_add_f32_e32 v98, v113, v98
	v_add_f32_e32 v98, v114, v98
	v_add_f32_e32 v98, v115, v98
	v_add_f32_e32 v98, v116, v98
	v_add_f32_e32 v98, v117, v98
	v_add_f32_e32 v98, v118, v98
	v_add_f32_e32 v98, v119, v98
	v_add_f32_e32 v98, v120, v98
	v_add_f32_e32 v98, v121, v98
	v_add_f32_e32 v98, v122, v98
	v_add_f32_e32 v98, v123, v98
	v_mov_b32_e32 v99, v98
	v_cvt_pk_bf16_f32 v100, v202, v221
	v_cvt_pk_bf16_f32 v101, v222, v223
	v_permlane32_swap_b32_e32 v98, v99
	v_permlane32_swap_b32_e32 v100, v102
	v_permlane32_swap_b32_e32 v101, v103
	v_cvt_pk_bf16_f32 v106, v193, v194
	v_cvt_pk_bf16_f32 v107, v195, v197
	v_cvt_pk_bf16_f32 v108, v108, v109
	v_cvt_pk_bf16_f32 v109, v110, v111
	v_cvt_pk_bf16_f32 v110, v112, v113
	v_cvt_pk_bf16_f32 v111, v114, v115
	v_cvt_pk_bf16_f32 v112, v116, v117
	v_cvt_pk_bf16_f32 v113, v118, v119
	v_cvt_pk_bf16_f32 v114, v120, v121
	v_cvt_pk_bf16_f32 v115, v122, v123
	v_permlane32_swap_b32_e32 v104, v106
	v_permlane32_swap_b32_e32 v105, v107
	v_permlane32_swap_b32_e32 v108, v110
	v_permlane32_swap_b32_e32 v109, v111
	v_permlane32_swap_b32_e32 v112, v114
	v_permlane32_swap_b32_e32 v113, v115
	ds_read_b64_tr_b16 v[116:117], v169 offset:0
	ds_read_b64_tr_b16 v[118:119], v169 offset:0x800
	ds_read_b64_tr_b16 v[120:121], v169 offset:0x1000
	ds_read_b64_tr_b16 v[122:123], v169 offset:0x1800
	ds_read_b64_tr_b16 v[124:125], v169 offset:0x2000
	ds_read_b64_tr_b16 v[126:127], v169 offset:0x2800
	ds_read_b64_tr_b16 v[128:129], v169 offset:0x3000
	ds_read_b64_tr_b16 v[130:131], v169 offset:0x3800
	s_nop 0
	s_waitcnt lgkmcnt(6)
	v_mfma_f32_32x32x16_bf16 v[0:15], v[100:103], v[116:119], v[0:15]
	ds_read_b64_tr_b16 v[116:117], v169 offset:0x200
	ds_read_b64_tr_b16 v[118:119], v169 offset:0xa00
	s_waitcnt lgkmcnt(6)
	v_mfma_f32_32x32x16_bf16 v[0:15], v[104:107], v[120:123], v[0:15]
	ds_read_b64_tr_b16 v[120:121], v169 offset:0x1200
	ds_read_b64_tr_b16 v[122:123], v169 offset:0x1a00
	s_waitcnt lgkmcnt(6)
	v_mfma_f32_32x32x16_bf16 v[0:15], v[108:111], v[124:127], v[0:15]
	ds_read_b64_tr_b16 v[124:125], v169 offset:0x2200
	ds_read_b64_tr_b16 v[126:127], v169 offset:0x2a00
	s_waitcnt lgkmcnt(6)
	v_mfma_f32_32x32x16_bf16 v[0:15], v[112:115], v[128:131], v[0:15]
	ds_read_b64_tr_b16 v[128:129], v169 offset:0x3200
	ds_read_b64_tr_b16 v[130:131], v169 offset:0x3a00
	s_waitcnt lgkmcnt(6)
	v_mfma_f32_32x32x16_bf16 v[48:63], v[100:103], v[116:119], v[48:63]
	ds_read_b64_tr_b16 v[116:117], v169 offset:0x400
	ds_read_b64_tr_b16 v[118:119], v169 offset:0xc00
	s_waitcnt lgkmcnt(6)
	v_mfma_f32_32x32x16_bf16 v[48:63], v[104:107], v[120:123], v[48:63]
	ds_read_b64_tr_b16 v[120:121], v169 offset:0x1400
	ds_read_b64_tr_b16 v[122:123], v169 offset:0x1c00
	s_waitcnt lgkmcnt(6)
	v_mfma_f32_32x32x16_bf16 v[48:63], v[108:111], v[124:127], v[48:63]
	ds_read_b64_tr_b16 v[124:125], v169 offset:0x2400
	ds_read_b64_tr_b16 v[126:127], v169 offset:0x2c00
	s_waitcnt lgkmcnt(6)
	v_mfma_f32_32x32x16_bf16 v[48:63], v[112:115], v[128:131], v[48:63]
	ds_read_b64_tr_b16 v[128:129], v169 offset:0x3400
	ds_read_b64_tr_b16 v[130:131], v169 offset:0x3c00
	s_waitcnt lgkmcnt(6)
	v_mfma_f32_32x32x16_bf16 v[32:47], v[100:103], v[116:119], v[32:47]
	ds_read_b64_tr_b16 v[116:117], v169 offset:0x600
	ds_read_b64_tr_b16 v[118:119], v169 offset:0xe00
	s_waitcnt lgkmcnt(6)
	v_mfma_f32_32x32x16_bf16 v[32:47], v[104:107], v[120:123], v[32:47]
	ds_read_b64_tr_b16 v[120:121], v169 offset:0x1600
	ds_read_b64_tr_b16 v[122:123], v169 offset:0x1e00
	s_waitcnt lgkmcnt(6)
	v_mfma_f32_32x32x16_bf16 v[32:47], v[108:111], v[124:127], v[32:47]
	ds_read_b64_tr_b16 v[124:125], v169 offset:0x2600
	ds_read_b64_tr_b16 v[126:127], v169 offset:0x2e00
	s_waitcnt lgkmcnt(6)
	v_mfma_f32_32x32x16_bf16 v[32:47], v[112:115], v[128:131], v[32:47]
	ds_read_b64_tr_b16 v[128:129], v169 offset:0x3600
	ds_read_b64_tr_b16 v[130:131], v169 offset:0x3e00
	s_waitcnt lgkmcnt(6)
	v_mfma_f32_32x32x16_bf16 v[16:31], v[100:103], v[116:119], v[16:31]
	v_max_f32_e32 v100, v81, v81
	v_max_f32_e32 v101, v80, v80
	v_max_f32_e32 v100, v101, v100
	v_max3_f32 v100, v100, v82, v83
	v_max3_f32 v100, v100, v84, v85
	v_max3_f32 v100, v100, v86, v87
	v_max3_f32 v100, v100, v88, v89
	v_max3_f32 v100, v100, v90, v91
	v_max3_f32 v100, v100, v92, v93
	s_waitcnt lgkmcnt(4)
	v_mfma_f32_32x32x16_bf16 v[16:31], v[104:107], v[120:123], v[16:31]
	v_max3_f32 v100, v100, v94, v95
	v_max3_f32 v100, v100, v64, v65
	v_max3_f32 v100, v100, v66, v67
	v_max3_f32 v100, v100, v68, v69
	v_max3_f32 v100, v100, v70, v71
	v_max3_f32 v100, v100, v72, v73
	v_max3_f32 v100, v100, v74, v75
	v_max3_f32 v100, v100, v76, v77
	s_waitcnt lgkmcnt(2)
	v_mfma_f32_32x32x16_bf16 v[16:31], v[108:111], v[124:127], v[16:31]
	v_max3_f32 v100, v100, v78, v79
	v_mov_b32_e32 v101, v100
	s_nop 1
	v_permlane32_swap_b32_e32 v100, v101
	v_max_f32_e32 v101, v101, v101
	v_max_f32_e32 v100, v100, v100
	v_max_f32_e32 v100, v100, v101
	v_sub_f32_e32 v101, v100, v186
	v_cmp_ge_f32_e32 vcc, s73, v101
	v_max_f32_e32 v101, v186, v186
	v_max_f32_e32 v101, v101, v100
	s_waitcnt lgkmcnt(0)
	v_mfma_f32_32x32x16_bf16 v[16:31], v[112:115], v[128:131], v[16:31]
	v_sub_f32_e32 v100, v186, v101
	v_mul_f32_e32 v100, 0x3e0293ee, v100
	v_exp_f32_e32 v100, v100
	s_cmp_eq_u64 vcc, exec
	s_cselect_b64 s[4:5], -1, 0
	v_cndmask_b32_e64 v100, v100, 1.0, s[4:5]
	v_cmp_gt_f32_e32 vcc, 1.0, v100
	s_barrier
	s_cbranch_vccz .LBB0_860
	s_and_saveexec_b64 s[8:9], s[2:3]
	ds_write_b32 v171, v100 offset:128
	s_or_b64 exec, exec, s[8:9]
	s_waitcnt lgkmcnt(0)
	v_add_u32_e32 v114, v168, v170
	ds_read_b128 v[102:105], v114 offset:224
	ds_read_b128 v[106:109], v114 offset:192
	ds_read_b128 v[110:113], v114 offset:160
	ds_read_b128 v[114:117], v114 offset:128
	s_waitcnt lgkmcnt(3)
	v_pk_mul_f32 v[12:13], v[12:13], v[102:103]
	s_waitcnt lgkmcnt(2)
	v_pk_mul_f32 v[8:9], v[8:9], v[106:107]
	s_waitcnt lgkmcnt(1)
	v_pk_mul_f32 v[4:5], v[4:5], v[110:111]
	v_pk_mul_f32 v[14:15], v[14:15], v[104:105]
	v_pk_mul_f32 v[10:11], v[10:11], v[108:109]
	v_pk_mul_f32 v[6:7], v[6:7], v[112:113]
	s_waitcnt lgkmcnt(0)
	v_pk_mul_f32 v[2:3], v[2:3], v[116:117]
	v_pk_mul_f32 v[0:1], v[0:1], v[114:115]
	v_pk_mul_f32 v[60:61], v[60:61], v[102:103]
	v_pk_mul_f32 v[56:57], v[56:57], v[106:107]
	v_pk_mul_f32 v[52:53], v[52:53], v[110:111]
	v_pk_mul_f32 v[62:63], v[62:63], v[104:105]
	v_pk_mul_f32 v[58:59], v[58:59], v[108:109]
	v_pk_mul_f32 v[54:55], v[54:55], v[112:113]
	v_pk_mul_f32 v[50:51], v[50:51], v[116:117]
	v_pk_mul_f32 v[48:49], v[48:49], v[114:115]
	v_pk_mul_f32 v[44:45], v[44:45], v[102:103]
	v_pk_mul_f32 v[40:41], v[40:41], v[106:107]
	v_pk_mul_f32 v[36:37], v[36:37], v[110:111]
	v_pk_mul_f32 v[46:47], v[46:47], v[104:105]
	v_pk_mul_f32 v[42:43], v[42:43], v[108:109]
	v_pk_mul_f32 v[38:39], v[38:39], v[112:113]
	v_pk_mul_f32 v[34:35], v[34:35], v[116:117]
	v_pk_mul_f32 v[32:33], v[32:33], v[114:115]
	v_pk_mul_f32 v[28:29], v[28:29], v[102:103]
	v_pk_mul_f32 v[24:25], v[24:25], v[106:107]
	v_pk_mul_f32 v[20:21], v[20:21], v[110:111]
	v_pk_mul_f32 v[30:31], v[30:31], v[104:105]
	v_pk_mul_f32 v[26:27], v[26:27], v[108:109]
	v_pk_mul_f32 v[22:23], v[22:23], v[112:113]
	v_pk_mul_f32 v[18:19], v[18:19], v[116:117]
	v_pk_mul_f32 v[16:17], v[16:17], v[114:115]
.LBB0_860:
	v_cndmask_b32_e64 v101, v101, v186, s[4:5]
	v_mul_f32_e32 v101, 0xbe0293ee, v101
	v_fmamk_f32 v80, v80, 0x3e0293ee, v101
	v_fmamk_f32 v81, v81, 0x3e0293ee, v101
	v_fmamk_f32 v110, v93, 0x3e0293ee, v101
	v_fmamk_f32 v93, v74, 0x3e0293ee, v101
	v_exp_f32_e32 v74, v80
	v_fmamk_f32 v82, v82, 0x3e0293ee, v101
	v_fmamk_f32 v111, v94, 0x3e0293ee, v101
	v_fmamk_f32 v94, v75, 0x3e0293ee, v101
	v_exp_f32_e32 v75, v81
	v_fmamk_f32 v83, v83, 0x3e0293ee, v101
	v_fmamk_f32 v112, v95, 0x3e0293ee, v101
	v_fmamk_f32 v95, v76, 0x3e0293ee, v101
	v_exp_f32_e32 v76, v82
	v_fmamk_f32 v84, v84, 0x3e0293ee, v101
	v_fmamk_f32 v64, v64, 0x3e0293ee, v101
	v_exp_f32_e32 v80, v83
	v_fmamk_f32 v102, v85, 0x3e0293ee, v101
	v_fmamk_f32 v103, v86, 0x3e0293ee, v101
	v_fmamk_f32 v104, v87, 0x3e0293ee, v101
	v_fmamk_f32 v105, v88, 0x3e0293ee, v101
	v_fmamk_f32 v106, v89, 0x3e0293ee, v101
	v_fmamk_f32 v107, v90, 0x3e0293ee, v101
	v_fmamk_f32 v108, v91, 0x3e0293ee, v101
	v_fmamk_f32 v109, v92, 0x3e0293ee, v101
	v_fmamk_f32 v65, v65, 0x3e0293ee, v101
	v_fmamk_f32 v85, v66, 0x3e0293ee, v101
	v_fmamk_f32 v86, v67, 0x3e0293ee, v101
	v_fmamk_f32 v87, v68, 0x3e0293ee, v101
	v_fmamk_f32 v88, v69, 0x3e0293ee, v101
	v_fmamk_f32 v89, v70, 0x3e0293ee, v101
	v_fmamk_f32 v90, v71, 0x3e0293ee, v101
	v_fmamk_f32 v91, v72, 0x3e0293ee, v101
	v_fmamk_f32 v92, v73, 0x3e0293ee, v101
	v_exp_f32_e32 v81, v84
	v_fmamk_f32 v77, v77, 0x3e0293ee, v101
	v_fmamk_f32 v78, v78, 0x3e0293ee, v101
	v_fmac_f32_e32 v101, 0x3e0293ee, v79
	v_exp_f32_e32 v79, v64
	v_add_f32_e32 v64, 0, v74
	v_exp_f32_e32 v82, v102
	v_add_f32_e32 v64, v75, v64
	v_exp_f32_e32 v83, v103
	v_add_f32_e32 v64, v76, v64
	v_exp_f32_e32 v84, v104
	v_add_f32_e32 v64, v80, v64
	v_exp_f32_e32 v66, v105
	v_add_f32_e32 v64, v81, v64
	v_exp_f32_e32 v67, v106
	v_add_f32_e32 v64, v82, v64
	v_exp_f32_e32 v68, v107
	v_add_f32_e32 v64, v83, v64
	v_exp_f32_e32 v69, v108
	v_add_f32_e32 v64, v84, v64
	v_exp_f32_e32 v70, v109
	v_add_f32_e32 v64, v66, v64
	v_exp_f32_e32 v71, v110
	v_add_f32_e32 v64, v67, v64
	v_exp_f32_e32 v72, v111
	v_add_f32_e32 v64, v68, v64
	v_exp_f32_e32 v73, v112
	v_add_f32_e32 v64, v69, v64
	v_add_f32_e32 v64, v70, v64
	v_exp_f32_e32 v102, v65
	v_add_f32_e32 v64, v71, v64
	v_exp_f32_e32 v85, v85
	v_add_f32_e32 v64, v72, v64
	v_exp_f32_e32 v86, v86
	v_add_f32_e32 v64, v73, v64
	v_exp_f32_e32 v87, v87
	v_add_f32_e32 v64, v79, v64
	v_exp_f32_e32 v88, v88
	v_add_f32_e32 v64, v102, v64
	v_exp_f32_e32 v89, v89
	v_add_f32_e32 v64, v85, v64
	v_exp_f32_e32 v90, v90
	v_add_f32_e32 v64, v86, v64
	v_exp_f32_e32 v91, v91
	v_add_f32_e32 v64, v87, v64
	v_exp_f32_e32 v92, v92
	v_add_f32_e32 v64, v88, v64
	v_exp_f32_e32 v93, v93
	v_add_f32_e32 v64, v89, v64
	v_exp_f32_e32 v94, v94
	v_add_f32_e32 v64, v90, v64
	v_exp_f32_e32 v95, v95
	v_add_f32_e32 v64, v91, v64
	v_exp_f32_e32 v103, v77
	v_add_f32_e32 v64, v92, v64
	v_exp_f32_e32 v104, v78
	v_add_f32_e32 v64, v93, v64
	v_exp_f32_e32 v101, v101
	v_add_f32_e32 v64, v94, v64
	v_add_f32_e32 v64, v95, v64
	v_add_f32_e32 v64, v103, v64
	v_add_f32_e32 v64, v104, v64
	v_add_f32_e32 v64, v101, v64
	v_mov_b32_e32 v65, v64
	s_nop 1
	v_permlane32_swap_b32_e32 v64, v65
	v_cvt_pk_bf16_f32 v74, v74, v75
	v_cvt_pk_bf16_f32 v75, v76, v80
	v_cvt_pk_bf16_f32 v76, v81, v82
	v_cvt_pk_bf16_f32 v77, v83, v84
	v_cvt_pk_bf16_f32 v66, v66, v67
	v_cvt_pk_bf16_f32 v67, v68, v69
	v_cvt_pk_bf16_f32 v68, v70, v71
	v_cvt_pk_bf16_f32 v69, v72, v73
	v_cvt_pk_bf16_f32 v70, v79, v102
	v_cvt_pk_bf16_f32 v71, v85, v86
	v_cvt_pk_bf16_f32 v72, v87, v88
	v_cvt_pk_bf16_f32 v73, v89, v90
	v_cvt_pk_bf16_f32 v78, v91, v92
	v_cvt_pk_bf16_f32 v79, v93, v94
	v_cvt_pk_bf16_f32 v80, v95, v103
	v_cvt_pk_bf16_f32 v81, v104, v101
	v_permlane32_swap_b32_e32 v74, v76
	v_permlane32_swap_b32_e32 v75, v77
	v_permlane32_swap_b32_e32 v66, v68
	v_permlane32_swap_b32_e32 v67, v69
	v_permlane32_swap_b32_e32 v70, v72
	v_permlane32_swap_b32_e32 v71, v73
	v_permlane32_swap_b32_e32 v78, v80
	v_permlane32_swap_b32_e32 v79, v81
	ds_read_b64_tr_b16 v[82:83], v172 offset:0
	ds_read_b64_tr_b16 v[84:85], v172 offset:0x800
	ds_read_b64_tr_b16 v[86:87], v172 offset:0x1000
	ds_read_b64_tr_b16 v[88:89], v172 offset:0x1800
	ds_read_b64_tr_b16 v[90:91], v172 offset:0x2000
	ds_read_b64_tr_b16 v[92:93], v172 offset:0x2800
	ds_read_b64_tr_b16 v[102:103], v172 offset:0x3000
	ds_read_b64_tr_b16 v[104:105], v172 offset:0x3800
	s_nop 0
	s_waitcnt lgkmcnt(6)
	v_mfma_f32_32x32x16_bf16 v[0:15], v[74:77], v[82:85], v[0:15]
	ds_read_b64_tr_b16 v[82:83], v172 offset:0x200
	ds_read_b64_tr_b16 v[84:85], v172 offset:0xa00
	s_waitcnt lgkmcnt(6)
	v_mfma_f32_32x32x16_bf16 v[0:15], v[66:69], v[86:89], v[0:15]
	ds_read_b64_tr_b16 v[86:87], v172 offset:0x1200
	ds_read_b64_tr_b16 v[88:89], v172 offset:0x1a00
	s_waitcnt lgkmcnt(6)
	v_mfma_f32_32x32x16_bf16 v[0:15], v[70:73], v[90:93], v[0:15]
	ds_read_b64_tr_b16 v[90:91], v172 offset:0x2200
	ds_read_b64_tr_b16 v[92:93], v172 offset:0x2a00
	s_waitcnt lgkmcnt(6)
	v_mfma_f32_32x32x16_bf16 v[0:15], v[78:81], v[102:105], v[0:15]
	ds_read_b64_tr_b16 v[102:103], v172 offset:0x3200
	ds_read_b64_tr_b16 v[104:105], v172 offset:0x3a00
	s_waitcnt lgkmcnt(6)
	v_mfma_f32_32x32x16_bf16 v[48:63], v[74:77], v[82:85], v[48:63]
	ds_read_b64_tr_b16 v[82:83], v172 offset:0x400
	ds_read_b64_tr_b16 v[84:85], v172 offset:0xc00
	s_waitcnt lgkmcnt(6)
	v_mfma_f32_32x32x16_bf16 v[48:63], v[66:69], v[86:89], v[48:63]
	ds_read_b64_tr_b16 v[86:87], v172 offset:0x1400
	ds_read_b64_tr_b16 v[88:89], v172 offset:0x1c00
	s_waitcnt lgkmcnt(6)
	v_mfma_f32_32x32x16_bf16 v[48:63], v[70:73], v[90:93], v[48:63]
	ds_read_b64_tr_b16 v[90:91], v172 offset:0x2400
	ds_read_b64_tr_b16 v[92:93], v172 offset:0x2c00
	s_waitcnt lgkmcnt(6)
	v_mfma_f32_32x32x16_bf16 v[48:63], v[78:81], v[102:105], v[48:63]
	ds_read_b64_tr_b16 v[102:103], v172 offset:0x3400
	ds_read_b64_tr_b16 v[104:105], v172 offset:0x3c00
	s_waitcnt lgkmcnt(6)
	v_mfma_f32_32x32x16_bf16 v[32:47], v[74:77], v[82:85], v[32:47]
	ds_read_b64_tr_b16 v[82:83], v172 offset:0x600
	ds_read_b64_tr_b16 v[84:85], v172 offset:0xe00
	s_waitcnt lgkmcnt(6)
	v_mfma_f32_32x32x16_bf16 v[32:47], v[66:69], v[86:89], v[32:47]
	ds_read_b64_tr_b16 v[86:87], v172 offset:0x1600
	ds_read_b64_tr_b16 v[88:89], v172 offset:0x1e00
	s_waitcnt lgkmcnt(6)
	v_mfma_f32_32x32x16_bf16 v[32:47], v[70:73], v[90:93], v[32:47]
	ds_read_b64_tr_b16 v[90:91], v172 offset:0x2600
	ds_read_b64_tr_b16 v[92:93], v172 offset:0x2e00
	s_waitcnt lgkmcnt(6)
	v_mfma_f32_32x32x16_bf16 v[32:47], v[78:81], v[102:105], v[32:47]
	ds_read_b64_tr_b16 v[102:103], v172 offset:0x3600
	ds_read_b64_tr_b16 v[104:105], v172 offset:0x3e00
	s_waitcnt lgkmcnt(6)
	v_mfma_f32_32x32x16_bf16 v[16:31], v[74:77], v[82:85], v[16:31]
	s_waitcnt lgkmcnt(4)
	v_mfma_f32_32x32x16_bf16 v[16:31], v[66:69], v[86:89], v[16:31]
	s_waitcnt lgkmcnt(2)
	v_mfma_f32_32x32x16_bf16 v[16:31], v[70:73], v[90:93], v[16:31]
	s_waitcnt lgkmcnt(0)
	v_mfma_f32_32x32x16_bf16 v[16:31], v[78:81], v[102:105], v[16:31]
	s_and_saveexec_b64 s[4:5], s[2:3]
	s_cbranch_execz .LBB0_839
	v_add_f32_e32 v66, v98, v99
	v_fmac_f32_e32 v66, v165, v189
	v_add_f32_e32 v64, v64, v65
	v_fmac_f32_e32 v64, v66, v100
	ds_write_b32 v171, v64
	s_branch .LBB0_839
